# v22 + no grid barrier between the PLE projection GEMM and layer 0's z GEMM (workgroup barrier kept; PP is first read after a later grid barrier)
# speedup vs baseline: 1.0568x; 1.0001x over previous
.LBB0_671:
	v_readlane_b32 s8, v253, 2
	v_readlane_b32 s11, v253, 5
	s_cmp_gt_u32 s11, 2
	s_cselect_b64 s[4:5], -1, 0
	s_and_b64 s[4:5], s[6:7], s[4:5]
	s_andn2_b64 vcc, exec, s[4:5]
	v_readlane_b32 s9, v253, 3
	v_readlane_b32 s10, v253, 4
	s_cbranch_vccnz .LBB0_721
	s_waitcnt vmcnt(0)
	v_cmp_eq_u32_e32 vcc, 0, v0
	s_waitcnt vmcnt(0) lgkmcnt(0)
	s_barrier
	s_and_saveexec_b64 s[4:5], vcc
	s_branch .LBB0_720
	v_readlane_b32 s3, v253, 8
	s_waitcnt vmcnt(0) expcnt(0) lgkmcnt(0)
	s_nop 0
	v_mov_b32_e32 v1, s3
	ds_read_b32 v3, v1
	ds_read_b32 v1, v1 offset:4
	s_waitcnt lgkmcnt(1)
	v_cmp_ne_u32_e32 vcc, 0, v3
	s_cbranch_vccnz .LBB0_688
	v_readlane_b32 s6, v253, 0
	v_readlane_b32 s7, v253, 1
	s_load_dwordx2 s[10:11], s[6:7], 0x4
	v_readlane_b32 s40, v253, 2
	v_readlane_b32 s41, v253, 3
	s_add_u32 s6, s40, 0x4200
	s_addc_u32 s7, s41, 0
	s_add_u32 s8, s40, 0x4400
	s_addc_u32 s9, s41, 0
	s_waitcnt lgkmcnt(0)
	s_mul_i32 s3, s10, s86
	s_add_u32 s10, s40, 0x4500
	s_mul_i32 s3, s3, s11
	s_addc_u32 s11, s41, 0
	s_add_u32 s12, s40, 0x4600
	s_addc_u32 s13, s41, 0
	s_add_u32 s14, s40, 0x4700
	s_addc_u32 s15, s41, 0
	s_add_u32 s16, s40, 0x4800
	s_addc_u32 s17, s41, 0
	s_add_u32 s18, s40, 0x4900
	s_addc_u32 s19, s41, 0
	s_add_u32 s20, s40, 0x4a00
	s_addc_u32 s21, s41, 0
	s_add_u32 s22, s40, 0x4b00
	s_addc_u32 s23, s41, 0
	s_add_u32 s24, s40, 0x4c00
	s_addc_u32 s25, s41, 0
	s_add_u32 s26, s40, 0x4d00
	s_addc_u32 s27, s41, 0
	s_add_u32 s28, s40, 0x4e00
	s_addc_u32 s29, s41, 0
	s_add_u32 s30, s40, 0x4f00
	s_addc_u32 s31, s41, 0
	s_add_u32 s34, s40, 0x5000
	s_addc_u32 s35, s41, 0
	s_add_u32 s36, s40, 0x5100
	s_addc_u32 s37, s41, 0
	s_add_u32 s38, s40, 0x5200
	s_addc_u32 s39, s41, 0
	s_add_u32 s40, s40, 0x5300
	s_addc_u32 s41, s41, 0
	s_mov_b32 s33, 1
	v_mov_b32_e32 v17, 0
	v_readlane_b32 s42, v253, 4
	v_readlane_b32 s43, v253, 5
	s_branch .LBB0_676
